# kv unit V^T stores via LDS transpose (16B rows) and dC/dR stores via DPP quad transposes (16B), on top of v15
# baseline (speedup 1.0000x reference)
.LBB0_548:
	s_or_b64 exec, exec, s[0:1]
	s_load_dwordx4 s[40:43], s[76:77], 0x158
	v_mov_b32_e32 v71, v195
	s_movk_i32 s0, 0x2100
	v_mul_f32_e32 v65, v82, v65
	v_mul_f32_e32 v61, v82, v61
	v_mul_f32_e32 v64, v82, v64
	v_mul_f32_e32 v60, v82, v60
	v_mul_f32_e32 v63, v82, v63
	v_mul_f32_e32 v59, v82, v59
	v_mul_f32_e32 v62, v82, v62
	v_mul_f32_e32 v58, v82, v58
	v_mul_f32_e32 v57, v82, v57
	v_mul_f32_e32 v53, v53, v82
	v_mul_f32_e32 v56, v82, v56
	v_mul_f32_e32 v52, v52, v82
	v_mul_f32_e32 v55, v82, v55
	v_mul_f32_e32 v51, v51, v82
	v_mul_f32_e32 v54, v82, v54
	v_mul_f32_e32 v50, v50, v82
	v_mul_f32_e32 v49, v49, v82
	v_mul_f32_e32 v45, v45, v82
	v_mul_f32_e32 v48, v48, v82
	v_mul_f32_e32 v44, v44, v82
	v_mul_f32_e32 v47, v47, v82
	v_mul_f32_e32 v43, v43, v82
	v_mul_f32_e32 v46, v46, v82
	v_mul_f32_e32 v42, v42, v82
	v_mul_f32_e32 v41, v41, v82
	v_mul_f32_e32 v37, v37, v82
	v_mul_f32_e32 v40, v40, v82
	v_mul_f32_e32 v36, v36, v82
	v_mul_f32_e32 v39, v39, v82
	v_mul_f32_e32 v35, v35, v82
	v_mul_f32_e32 v38, v38, v82
	v_mul_f32_e32 v34, v34, v82
	v_mul_f32_e32 v82, v2, v97
	v_mul_f32_e32 v83, v3, v97
	v_mul_f32_e32 v86, v4, v97
	v_mul_f32_e32 v87, v5, v97
	v_mad_i64_i32 v[2:3], s[0:1], v92, s0, v[70:71]
	s_waitcnt lgkmcnt(0)
	v_mov_b64_e32 v[4:5], s[40:41]
	v_mad_u64_u32 v[4:5], s[0:1], v2, s24, v[4:5]
	v_mad_i32_i24 v5, v3, s24, v5
	s_mul_i32 s70, s29, 0xc0
	v_lshl_add_u64 v[2:3], v[4:5], 0, s[70:71]
	v_mul_f32_e32 v37, v101, v37
	v_mul_f32_e32 v36, v100, v36
	v_mul_f32_e32 v35, v99, v35
	v_mul_f32_e32 v34, v98, v34
	v_lshl_add_u64 v[2:3], v[2:3], 0, v[194:195]
	v_cvt_pk_bf16_f32 v4, v34, v35
	v_cvt_pk_bf16_f32 v5, v36, v37
	v_mul_f32_e32 v41, v113, v41
	v_mul_f32_e32 v40, v110, v40
	v_mul_f32_e32 v39, v108, v39
	v_mul_f32_e32 v38, v106, v38
	global_store_dwordx2 v[2:3], v[4:5], off
	v_cvt_pk_bf16_f32 v4, v38, v39
	v_cvt_pk_bf16_f32 v5, v40, v41
	global_store_dwordx2 v[2:3], v[4:5], off offset:64
	v_cvt_pk_bf16_f32 v4, v80, v81
	v_cvt_pk_bf16_f32 v5, v84, v85
	v_mul_f32_e32 v45, v105, v45
	v_mul_f32_e32 v44, v104, v44
	v_mul_f32_e32 v43, v103, v43
	v_mul_f32_e32 v42, v102, v42
	global_store_dwordx2 v[2:3], v[4:5], off offset:128
	v_cvt_pk_bf16_f32 v4, v42, v43
	v_cvt_pk_bf16_f32 v5, v44, v45
	v_mul_f32_e32 v49, v121, v49
	v_mul_f32_e32 v48, v119, v48
	v_mul_f32_e32 v47, v117, v47
	v_mul_f32_e32 v46, v115, v46
	global_store_dwordx2 v[2:3], v[4:5], off offset:16
	v_cvt_pk_bf16_f32 v4, v46, v47
	v_cvt_pk_bf16_f32 v5, v48, v49
	global_store_dwordx2 v[2:3], v[4:5], off offset:80
	v_cvt_pk_bf16_f32 v4, v78, v79
	v_cvt_pk_bf16_f32 v5, v74, v75
	v_mul_f32_e32 v53, v114, v53
	v_mul_f32_e32 v52, v112, v52
	v_mul_f32_e32 v51, v109, v51
	v_mul_f32_e32 v50, v107, v50
	global_store_dwordx2 v[2:3], v[4:5], off offset:144
	v_cvt_pk_bf16_f32 v4, v50, v51
	v_cvt_pk_bf16_f32 v5, v52, v53
	v_mul_f32_e32 v57, v127, v57
	v_mul_f32_e32 v56, v126, v56
	v_mul_f32_e32 v55, v125, v55
	v_mul_f32_e32 v54, v123, v54
	global_store_dwordx2 v[2:3], v[4:5], off offset:32
	v_cvt_pk_bf16_f32 v4, v54, v55
	v_cvt_pk_bf16_f32 v5, v56, v57
	global_store_dwordx2 v[2:3], v[4:5], off offset:96
	v_cvt_pk_bf16_f32 v4, v76, v77
	v_cvt_pk_bf16_f32 v5, v68, v69
	v_mul_f32_e32 v61, v124, v61
	v_mul_f32_e32 v60, v122, v60
	v_mul_f32_e32 v59, v118, v59
	v_mul_f32_e32 v58, v116, v58
	global_store_dwordx2 v[2:3], v[4:5], off offset:160
	v_cvt_pk_bf16_f32 v4, v58, v59
	v_cvt_pk_bf16_f32 v5, v60, v61
	v_mul_f32_e32 v65, v131, v65
	v_mul_f32_e32 v64, v130, v64
	v_mul_f32_e32 v63, v129, v63
	v_mul_f32_e32 v62, v128, v62
	global_store_dwordx2 v[2:3], v[4:5], off offset:48
	v_cvt_pk_bf16_f32 v4, v62, v63
	v_cvt_pk_bf16_f32 v5, v64, v65
	global_store_dwordx2 v[2:3], v[4:5], off offset:112
	v_cvt_pk_bf16_f32 v4, v66, v67
	v_cvt_pk_bf16_f32 v5, v72, v73
	global_store_dwordx2 v[2:3], v[4:5], off offset:176
	v_and_b32_e32 v34, 63, v0
	v_lshrrev_b32_e32 v35, 6, v0
	v_mul_u32_u24_e32 v35, 0x1400, v35
	v_add_u32_e32 v35, 64, v35
	v_and_b32_e32 v36, 31, v70
	v_lshlrev_b32_e32 v37, 1, v36
	v_and_b32_e32 v37, 8, v37
	v_lshrrev_b32_e32 v38, 1, v36
	v_and_b32_e32 v38, 4, v38
	v_and_b32_e32 v36, 19, v36
	v_or3_b32 v36, v36, v37, v38
	v_mul_u32_u24_e32 v37, 0x50, v96
	v_lshl_add_u32 v36, v36, 1, v37
	v_add_u32_e32 v36, v36, v35
	v_cvt_pk_bf16_f32 v39, v82, v195
	ds_write_b16 v36, v39 offset:0
	v_cvt_pk_bf16_f32 v40, v83, v195
	ds_write_b16 v36, v40 offset:80
	v_cvt_pk_bf16_f32 v41, v86, v195
	ds_write_b16 v36, v41 offset:160
	v_cvt_pk_bf16_f32 v42, v87, v195
	ds_write_b16 v36, v42 offset:240
	v_mul_f32_e32 v39, v6, v97
	v_cvt_pk_bf16_f32 v39, v39, v195
	ds_write_b16 v36, v39 offset:640
	v_mul_f32_e32 v40, v7, v97
	v_cvt_pk_bf16_f32 v40, v40, v195
	ds_write_b16 v36, v40 offset:720
	v_mul_f32_e32 v41, v8, v97
	v_cvt_pk_bf16_f32 v41, v41, v195
	ds_write_b16 v36, v41 offset:800
	v_mul_f32_e32 v42, v9, v97
	v_cvt_pk_bf16_f32 v42, v42, v195
	ds_write_b16 v36, v42 offset:880
	v_mul_f32_e32 v39, v10, v97
	v_cvt_pk_bf16_f32 v39, v39, v195
	ds_write_b16 v36, v39 offset:1280
	v_mul_f32_e32 v40, v11, v97
	v_cvt_pk_bf16_f32 v40, v40, v195
	ds_write_b16 v36, v40 offset:1360
	v_mul_f32_e32 v41, v12, v97
	v_cvt_pk_bf16_f32 v41, v41, v195
	ds_write_b16 v36, v41 offset:1440
	v_mul_f32_e32 v42, v13, v97
	v_cvt_pk_bf16_f32 v42, v42, v195
	ds_write_b16 v36, v42 offset:1520
	v_mul_f32_e32 v39, v14, v97
	v_cvt_pk_bf16_f32 v39, v39, v195
	ds_write_b16 v36, v39 offset:1920
	v_mul_f32_e32 v40, v15, v97
	v_cvt_pk_bf16_f32 v40, v40, v195
	ds_write_b16 v36, v40 offset:2000
	v_mul_f32_e32 v41, v16, v97
	v_cvt_pk_bf16_f32 v41, v41, v195
	ds_write_b16 v36, v41 offset:2080
	v_mul_f32_e32 v42, v17, v97
	v_cvt_pk_bf16_f32 v42, v42, v195
	ds_write_b16 v36, v42 offset:2160
	v_mul_f32_e32 v39, v18, v97
	v_cvt_pk_bf16_f32 v39, v39, v195
	ds_write_b16 v36, v39 offset:2560
	v_mul_f32_e32 v40, v19, v97
	v_cvt_pk_bf16_f32 v40, v40, v195
	ds_write_b16 v36, v40 offset:2640
	v_mul_f32_e32 v41, v20, v97
	v_cvt_pk_bf16_f32 v41, v41, v195
	ds_write_b16 v36, v41 offset:2720
	v_mul_f32_e32 v42, v21, v97
	v_cvt_pk_bf16_f32 v42, v42, v195
	ds_write_b16 v36, v42 offset:2800
	v_mul_f32_e32 v39, v22, v97
	v_cvt_pk_bf16_f32 v39, v39, v195
	ds_write_b16 v36, v39 offset:3200
	v_mul_f32_e32 v40, v23, v97
	v_cvt_pk_bf16_f32 v40, v40, v195
	ds_write_b16 v36, v40 offset:3280
	v_mul_f32_e32 v41, v24, v97
	v_cvt_pk_bf16_f32 v41, v41, v195
	ds_write_b16 v36, v41 offset:3360
	v_mul_f32_e32 v42, v25, v97
	v_cvt_pk_bf16_f32 v42, v42, v195
	ds_write_b16 v36, v42 offset:3440
	v_mul_f32_e32 v39, v26, v97
	v_cvt_pk_bf16_f32 v39, v39, v195
	ds_write_b16 v36, v39 offset:3840
	v_mul_f32_e32 v40, v27, v97
	v_cvt_pk_bf16_f32 v40, v40, v195
	ds_write_b16 v36, v40 offset:3920
	v_mul_f32_e32 v41, v28, v97
	v_cvt_pk_bf16_f32 v41, v41, v195
	ds_write_b16 v36, v41 offset:4000
	v_mul_f32_e32 v42, v29, v97
	v_cvt_pk_bf16_f32 v42, v42, v195
	ds_write_b16 v36, v42 offset:4080
	v_mul_f32_e32 v39, v30, v97
	v_cvt_pk_bf16_f32 v39, v39, v195
	ds_write_b16 v36, v39 offset:4480
	v_mul_f32_e32 v40, v31, v97
	v_cvt_pk_bf16_f32 v40, v40, v195
	ds_write_b16 v36, v40 offset:4560
	v_mul_f32_e32 v41, v32, v97
	v_cvt_pk_bf16_f32 v41, v41, v195
	ds_write_b16 v36, v41 offset:4640
	v_mul_f32_e32 v42, v33, v97
	v_cvt_pk_bf16_f32 v42, v42, v195
	ds_write_b16 v36, v42 offset:4720
	v_lshrrev_b32_e32 v37, 2, v34
	v_and_b32_e32 v38, 3, v34
	v_mul_u32_u24_e32 v56, 0x50, v37
	v_lshl_add_u32 v56, v38, 4, v56
	v_add_u32_e32 v56, v56, v35
	s_waitcnt lgkmcnt(0)
	ds_read_b128 v[40:43], v56 offset:0
	ds_read_b128 v[44:47], v56 offset:1280
	ds_read_b128 v[48:51], v56 offset:2560
	ds_read_b128 v[52:55], v56 offset:3840
	v_lshl_or_b32 v4, v92, 3, s29
	v_mov_b64_e32 v[2:3], s[42:43]
	s_mov_b32 s0, 0x108000
	v_mad_i64_i32 v[2:3], s[0:1], v4, s0, v[2:3]
	v_and_b32_e32 v58, 0xffffffe0, v70
	v_lshlrev_b32_e32 v58, 1, v58
	v_lshl_add_u32 v58, v38, 4, v58
	v_mul_u32_u24_e32 v57, 0x4200, v37
	v_add_u32_e32 v58, v58, v57
	v_mov_b32_e32 v59, 0
	v_lshl_add_u64 v[2:3], v[2:3], 0, v[58:59]
	s_mov_b32 s0, 0x42000
	s_mov_b32 s1, 0
	s_waitcnt lgkmcnt(3)
	global_store_dwordx4 v[2:3], v[40:43], off
	v_lshl_add_u64 v[2:3], v[2:3], 0, s[0:1]
	s_waitcnt lgkmcnt(2)
	global_store_dwordx4 v[2:3], v[44:47], off
	v_lshl_add_u64 v[2:3], v[2:3], 0, s[0:1]
	s_waitcnt lgkmcnt(1)
	global_store_dwordx4 v[2:3], v[48:51], off
	v_lshl_add_u64 v[2:3], v[2:3], 0, s[0:1]
	s_waitcnt lgkmcnt(0)
	global_store_dwordx4 v[2:3], v[52:55], off

.LBB0_595:
	s_or_b64 exec, exec, s[0:1]
	s_waitcnt lgkmcnt(0)
	s_barrier
	v_mov_b32 v18, v0
	s_and_b64 s[0:1], s[56:57], exec
	v_and_b32_e32 v28, 31, v18
	v_bfe_u32 v31, v18, 7, 1
	v_ashrrev_i32_e32 v19, 6, v18
	v_bfe_u32 v29, v18, 5, 1
	v_lshl_or_b32 v2, v31, 5, v28
	v_ashrrev_i32_e32 v30, 8, v18
	v_mul_u32_u24_e32 v2, 0x110, v2
	v_lshlrev_b32_e32 v3, 4, v29
	v_lshlrev_b32_e32 v4, 5, v19
	s_cselect_b32 s0, 0x41, 1
	v_add3_u32 v32, 0, v2, v3
	v_lshlrev_b32_e32 v2, 6, v30
	v_and_b32_e32 v33, 32, v4
	s_sub_i32 s9, s0, s34
	v_or3_b32 v2, v33, v2, v28
	s_movk_i32 s0, 0x110
	v_mul_lo_u32 v2, v2, s0
	v_add3_u32 v34, 0, v2, v3
	ds_read_b128 v[2:5], v32 offset:64
	ds_read_b128 v[20:23], v32 offset:96
	ds_read_b128 v[6:9], v34 offset:17472
	ds_read_b128 v[24:27], v34 offset:17504
	s_waitcnt lgkmcnt(1)
	v_mfma_f32_32x32x16_bf16 v[2:17], v[2:5], v[6:9], 0
	v_cmp_gt_u32_e32 vcc, s18, v18
	s_movk_i32 s30, 0x42
	v_lshlrev_b32_e32 v194, 2, v33
	s_waitcnt lgkmcnt(0)
	v_mfma_f32_32x32x16_bf16 v[2:17], v[20:23], v[24:27], v[2:17]
	ds_read_b128 v[20:23], v32 offset:128
	ds_read_b128 v[24:27], v34 offset:17536
	s_waitcnt lgkmcnt(0)
	v_mfma_f32_32x32x16_bf16 v[2:17], v[20:23], v[24:27], v[2:17]
	ds_read_b128 v[20:23], v32 offset:160
	ds_read_b128 v[24:27], v34 offset:17568
	s_waitcnt lgkmcnt(0)
	v_mfma_f32_32x32x16_bf16 v[2:17], v[20:23], v[24:27], v[2:17]
	ds_read_b128 v[20:23], v32 offset:192
	ds_read_b128 v[24:27], v34 offset:17600
	s_waitcnt lgkmcnt(0)
	v_mfma_f32_32x32x16_bf16 v[2:17], v[20:23], v[24:27], v[2:17]
	ds_read_b128 v[20:23], v32 offset:224
	ds_read_b128 v[24:27], v34 offset:17632
	s_waitcnt lgkmcnt(0)
	v_mfma_f32_32x32x16_bf16 v[2:17], v[20:23], v[24:27], v[2:17]
	ds_read_b128 v[20:23], v32 offset:256
	ds_read_b128 v[24:27], v34 offset:17664
	s_waitcnt lgkmcnt(0)
	v_mfma_f32_32x32x16_bf16 v[2:17], v[20:23], v[24:27], v[2:17]
	ds_read_b128 v[20:23], v32 offset:288
	ds_read_b128 v[24:27], v34 offset:17696
	s_load_dwordx2 s[0:1], s[76:77], 0x180
	s_waitcnt lgkmcnt(0)
	v_mfma_f32_32x32x16_bf16 v[2:17], v[20:23], v[24:27], v[2:17]
	v_mov_b32_e32 v20, s9
	v_mov_b32_e32 v21, s14
	v_cndmask_b32_e32 v20, v20, v21, vcc
	v_add_u32_e32 v21, s15, v30
	v_mul_lo_u32 v22, v21, s30
	v_ashrrev_i32_e32 v23, 31, v22
	v_ashrrev_i32_e32 v21, 31, v20
	v_lshl_add_u64 v[20:21], v[22:23], 0, v[20:21]
	v_lshlrev_b64 v[20:21], 14, v[20:21]
	v_lshl_add_u64 v[20:21], s[0:1], 0, v[20:21]
	v_lshl_add_u64 v[20:21], v[20:21], 0, v[194:195]
	v_lshlrev_b32_e32 v194, 2, v28
	v_lshlrev_b32_e32 v22, 13, v31
	v_lshl_add_u64 v[20:21], v[20:21], 0, v[194:195]
	v_lshl_or_b32 v194, v29, 10, v22
	v_lshl_add_u64 v[20:21], v[20:21], 0, v[194:195]
	s_mov_b32 vcc_lo, 0xaaaaaaaa
	s_mov_b32 vcc_hi, 0xaaaaaaaa
	s_mov_b32 s0, 0xcccccccc
	s_mov_b32 s1, 0xcccccccc
	v_and_b32_e32 v194, 3, v0
	v_mul_u32_u24_e32 v194, 0xfc, v194
	v_lshl_add_u64 v[20:21], v[20:21], 0, v[194:195]
	v_mov_b32_dpp v24, v3 quad_perm:[1,0,3,2] row_mask:0xf bank_mask:0xf bound_ctrl:1
	v_mov_b32_dpp v25, v2 quad_perm:[1,0,3,2] row_mask:0xf bank_mask:0xf bound_ctrl:1
	v_cndmask_b32_e32 v2, v2, v24, vcc
	v_cndmask_b32_e32 v3, v25, v3, vcc
	v_mov_b32_dpp v24, v5 quad_perm:[1,0,3,2] row_mask:0xf bank_mask:0xf bound_ctrl:1
	v_mov_b32_dpp v25, v4 quad_perm:[1,0,3,2] row_mask:0xf bank_mask:0xf bound_ctrl:1
	v_cndmask_b32_e32 v4, v4, v24, vcc
	v_cndmask_b32_e32 v5, v25, v5, vcc
	v_mov_b32_dpp v24, v7 quad_perm:[1,0,3,2] row_mask:0xf bank_mask:0xf bound_ctrl:1
	v_mov_b32_dpp v25, v6 quad_perm:[1,0,3,2] row_mask:0xf bank_mask:0xf bound_ctrl:1
	v_cndmask_b32_e32 v6, v6, v24, vcc
	v_cndmask_b32_e32 v7, v25, v7, vcc
	v_mov_b32_dpp v24, v9 quad_perm:[1,0,3,2] row_mask:0xf bank_mask:0xf bound_ctrl:1
	v_mov_b32_dpp v25, v8 quad_perm:[1,0,3,2] row_mask:0xf bank_mask:0xf bound_ctrl:1
	v_cndmask_b32_e32 v8, v8, v24, vcc
	v_cndmask_b32_e32 v9, v25, v9, vcc
	v_mov_b32_dpp v24, v11 quad_perm:[1,0,3,2] row_mask:0xf bank_mask:0xf bound_ctrl:1
	v_mov_b32_dpp v25, v10 quad_perm:[1,0,3,2] row_mask:0xf bank_mask:0xf bound_ctrl:1
	v_cndmask_b32_e32 v10, v10, v24, vcc
	v_cndmask_b32_e32 v11, v25, v11, vcc
	v_mov_b32_dpp v24, v13 quad_perm:[1,0,3,2] row_mask:0xf bank_mask:0xf bound_ctrl:1
	v_mov_b32_dpp v25, v12 quad_perm:[1,0,3,2] row_mask:0xf bank_mask:0xf bound_ctrl:1
	v_cndmask_b32_e32 v12, v12, v24, vcc
	v_cndmask_b32_e32 v13, v25, v13, vcc
	v_mov_b32_dpp v24, v15 quad_perm:[1,0,3,2] row_mask:0xf bank_mask:0xf bound_ctrl:1
	v_mov_b32_dpp v25, v14 quad_perm:[1,0,3,2] row_mask:0xf bank_mask:0xf bound_ctrl:1
	v_cndmask_b32_e32 v14, v14, v24, vcc
	v_cndmask_b32_e32 v15, v25, v15, vcc
	v_mov_b32_dpp v24, v17 quad_perm:[1,0,3,2] row_mask:0xf bank_mask:0xf bound_ctrl:1
	v_mov_b32_dpp v25, v16 quad_perm:[1,0,3,2] row_mask:0xf bank_mask:0xf bound_ctrl:1
	v_cndmask_b32_e32 v16, v16, v24, vcc
	v_cndmask_b32_e32 v17, v25, v17, vcc
	v_mov_b32_dpp v24, v4 quad_perm:[2,3,0,1] row_mask:0xf bank_mask:0xf bound_ctrl:1
	v_mov_b32_dpp v25, v2 quad_perm:[2,3,0,1] row_mask:0xf bank_mask:0xf bound_ctrl:1
	v_cndmask_b32_e64 v2, v2, v24, s[0:1]
	v_cndmask_b32_e64 v4, v25, v4, s[0:1]
	v_mov_b32_dpp v24, v5 quad_perm:[2,3,0,1] row_mask:0xf bank_mask:0xf bound_ctrl:1
	v_mov_b32_dpp v25, v3 quad_perm:[2,3,0,1] row_mask:0xf bank_mask:0xf bound_ctrl:1
	v_cndmask_b32_e64 v3, v3, v24, s[0:1]
	v_cndmask_b32_e64 v5, v25, v5, s[0:1]
	v_mov_b32_dpp v24, v8 quad_perm:[2,3,0,1] row_mask:0xf bank_mask:0xf bound_ctrl:1
	v_mov_b32_dpp v25, v6 quad_perm:[2,3,0,1] row_mask:0xf bank_mask:0xf bound_ctrl:1
	v_cndmask_b32_e64 v6, v6, v24, s[0:1]
	v_cndmask_b32_e64 v8, v25, v8, s[0:1]
	v_mov_b32_dpp v24, v9 quad_perm:[2,3,0,1] row_mask:0xf bank_mask:0xf bound_ctrl:1
	v_mov_b32_dpp v25, v7 quad_perm:[2,3,0,1] row_mask:0xf bank_mask:0xf bound_ctrl:1
	v_cndmask_b32_e64 v7, v7, v24, s[0:1]
	v_cndmask_b32_e64 v9, v25, v9, s[0:1]
	v_mov_b32_dpp v24, v12 quad_perm:[2,3,0,1] row_mask:0xf bank_mask:0xf bound_ctrl:1
	v_mov_b32_dpp v25, v10 quad_perm:[2,3,0,1] row_mask:0xf bank_mask:0xf bound_ctrl:1
	v_cndmask_b32_e64 v10, v10, v24, s[0:1]
	v_cndmask_b32_e64 v12, v25, v12, s[0:1]
	v_mov_b32_dpp v24, v13 quad_perm:[2,3,0,1] row_mask:0xf bank_mask:0xf bound_ctrl:1
	v_mov_b32_dpp v25, v11 quad_perm:[2,3,0,1] row_mask:0xf bank_mask:0xf bound_ctrl:1
	v_cndmask_b32_e64 v11, v11, v24, s[0:1]
	v_cndmask_b32_e64 v13, v25, v13, s[0:1]
	v_mov_b32_dpp v24, v16 quad_perm:[2,3,0,1] row_mask:0xf bank_mask:0xf bound_ctrl:1
	v_mov_b32_dpp v25, v14 quad_perm:[2,3,0,1] row_mask:0xf bank_mask:0xf bound_ctrl:1
	v_cndmask_b32_e64 v14, v14, v24, s[0:1]
	v_cndmask_b32_e64 v16, v25, v16, s[0:1]
	v_mov_b32_dpp v24, v17 quad_perm:[2,3,0,1] row_mask:0xf bank_mask:0xf bound_ctrl:1
	v_mov_b32_dpp v25, v15 quad_perm:[2,3,0,1] row_mask:0xf bank_mask:0xf bound_ctrl:1
	v_cndmask_b32_e64 v15, v15, v24, s[0:1]
	v_cndmask_b32_e64 v17, v25, v17, s[0:1]
	s_movk_i32 s0, 0x1000
	s_mov_b32 s1, 0
	v_lshl_add_u64 v[22:23], v[20:21], 0, s[0:1]
	global_store_dwordx4 v[20:21], v[2:5], off
	global_store_dwordx4 v[20:21], v[6:9], off offset:2048
	global_store_dwordx4 v[22:23], v[10:13], off
	global_store_dwordx4 v[22:23], v[14:17], off offset:2048
	v_cmp_gt_i32_e32 vcc, s20, v18
	s_and_saveexec_b64 s[0:1], vcc
	s_cbranch_execz .LBB0_599
	s_movk_i32 s30, 0x110
	v_mul_lo_u32 v3, v18, s30
	v_readlane_b32 s30, v254, 48
	v_and_b32_e32 v2, 63, v18
	v_mov_b32_e32 v4, 0
	v_add_u32_e32 v3, s30, v3
	s_mov_b32 s30, 0

.LBB0_599:
	s_or_b64 exec, exec, s[0:1]
	v_mov_b32 v18, v0
	s_nop 0
	v_and_b32_e32 v2, 64, v18
	v_cmp_eq_u32_e32 vcc, 0, v2
	s_and_saveexec_b64 s[0:1], vcc
	s_xor_b64 s[0:1], exec, s[0:1]
	s_cbranch_execz .LBB0_601
	v_bfe_u32 v33, v18, 7, 1
	v_and_b32_e32 v36, 31, v18
	v_bfe_u32 v35, v18, 5, 1
	v_lshl_or_b32 v2, v33, 5, v36
	v_mul_u32_u24_e32 v2, 0x110, v2
	v_lshlrev_b32_e32 v6, 4, v35
	v_add3_u32 v37, 0, v2, v6
	v_ashrrev_i32_e32 v34, 8, v18
	ds_read_b128 v[2:5], v37 offset:57408
	v_lshl_or_b32 v7, v34, 5, v36
	s_movk_i32 s30, 0x110
	v_mul_lo_u32 v7, v7, s30
	v_readlane_b32 s30, v254, 47
	v_cmp_gt_u32_e32 vcc, s18, v18
	v_lshlrev_b32_e32 v194, 2, v36
	v_add3_u32 v38, s30, v7, v6
	ds_read_b128 v[6:9], v38
	s_waitcnt lgkmcnt(0)
	v_mfma_f32_32x32x16_bf16 v[2:17], v[2:5], v[6:9], 0
	ds_read_b128 v[20:23], v37 offset:57440
	ds_read_b128 v[24:27], v38 offset:32
	s_waitcnt lgkmcnt(0)
	v_mfma_f32_32x32x16_bf16 v[2:17], v[20:23], v[24:27], v[2:17]
	ds_read_b128 v[20:23], v37 offset:57472
	ds_read_b128 v[24:27], v38 offset:64
	s_waitcnt lgkmcnt(0)
	v_mfma_f32_32x32x16_bf16 v[2:17], v[20:23], v[24:27], v[2:17]
	ds_read_b128 v[20:23], v37 offset:57504
	ds_read_b128 v[24:27], v38 offset:96
	s_waitcnt lgkmcnt(0)
	v_mfma_f32_32x32x16_bf16 v[2:17], v[20:23], v[24:27], v[2:17]
	ds_read_b128 v[20:23], v37 offset:57536
	ds_read_b128 v[24:27], v38 offset:128
	ds_read_b128 v[28:31], v37 offset:57568
	s_load_dwordx2 s[30:31], s[76:77], 0x1a8
	s_waitcnt lgkmcnt(0)
	v_mfma_f32_32x32x16_bf16 v[2:17], v[20:23], v[24:27], v[2:17]
	ds_read_b128 v[18:21], v38 offset:160
	v_mov_b32_e32 v22, s9
	v_mov_b32_e32 v23, s14
	v_cndmask_b32_e32 v32, v22, v23, vcc
	ds_read_b128 v[22:25], v37 offset:57600
	v_add_u32_e32 v26, s15, v34
	s_movk_i32 s9, 0x42
	s_waitcnt lgkmcnt(1)
	v_mfma_f32_32x32x16_bf16 v[2:17], v[28:31], v[18:21], v[2:17]
	ds_read_b128 v[18:21], v38 offset:192
	v_mul_lo_u32 v30, v26, s9
	ds_read_b128 v[26:29], v37 offset:57632
	v_lshlrev_b32_e32 v34, 12, v33
	v_ashrrev_i32_e32 v33, 31, v32
	v_ashrrev_i32_e32 v31, 31, v30
	s_waitcnt lgkmcnt(1)
	v_mfma_f32_32x32x16_bf16 v[2:17], v[22:25], v[18:21], v[2:17]
	ds_read_b128 v[18:21], v38 offset:224
	v_lshl_add_u64 v[22:23], v[30:31], 0, v[32:33]
	v_lshlrev_b64 v[22:23], 13, v[22:23]
	v_lshl_add_u64 v[22:23], s[30:31], 0, v[22:23]
	v_lshl_add_u64 v[22:23], v[22:23], 0, v[194:195]
	v_lshl_or_b32 v194, v35, 9, v34
	v_lshl_add_u64 v[22:23], v[22:23], 0, v[194:195]
	s_waitcnt lgkmcnt(0)
	v_mfma_f32_32x32x16_bf16 v[2:17], v[26:29], v[18:21], v[2:17]
	s_nop 11
	s_mov_b32 vcc_lo, 0xaaaaaaaa
	s_mov_b32 vcc_hi, 0xaaaaaaaa
	s_mov_b32 s30, 0xcccccccc
	s_mov_b32 s31, 0xcccccccc
	v_and_b32_e32 v194, 3, v0
	v_mul_u32_u24_e32 v194, 0x7c, v194
	v_lshl_add_u64 v[22:23], v[22:23], 0, v[194:195]
	v_mov_b32_dpp v24, v3 quad_perm:[1,0,3,2] row_mask:0xf bank_mask:0xf bound_ctrl:1
	v_mov_b32_dpp v25, v2 quad_perm:[1,0,3,2] row_mask:0xf bank_mask:0xf bound_ctrl:1
	v_cndmask_b32_e32 v2, v2, v24, vcc
	v_cndmask_b32_e32 v3, v25, v3, vcc
	v_mov_b32_dpp v24, v5 quad_perm:[1,0,3,2] row_mask:0xf bank_mask:0xf bound_ctrl:1
	v_mov_b32_dpp v25, v4 quad_perm:[1,0,3,2] row_mask:0xf bank_mask:0xf bound_ctrl:1
	v_cndmask_b32_e32 v4, v4, v24, vcc
	v_cndmask_b32_e32 v5, v25, v5, vcc
	v_mov_b32_dpp v24, v7 quad_perm:[1,0,3,2] row_mask:0xf bank_mask:0xf bound_ctrl:1
	v_mov_b32_dpp v25, v6 quad_perm:[1,0,3,2] row_mask:0xf bank_mask:0xf bound_ctrl:1
	v_cndmask_b32_e32 v6, v6, v24, vcc
	v_cndmask_b32_e32 v7, v25, v7, vcc
	v_mov_b32_dpp v24, v9 quad_perm:[1,0,3,2] row_mask:0xf bank_mask:0xf bound_ctrl:1
	v_mov_b32_dpp v25, v8 quad_perm:[1,0,3,2] row_mask:0xf bank_mask:0xf bound_ctrl:1
	v_cndmask_b32_e32 v8, v8, v24, vcc
	v_cndmask_b32_e32 v9, v25, v9, vcc
	v_mov_b32_dpp v24, v11 quad_perm:[1,0,3,2] row_mask:0xf bank_mask:0xf bound_ctrl:1
	v_mov_b32_dpp v25, v10 quad_perm:[1,0,3,2] row_mask:0xf bank_mask:0xf bound_ctrl:1
	v_cndmask_b32_e32 v10, v10, v24, vcc
	v_cndmask_b32_e32 v11, v25, v11, vcc
	v_mov_b32_dpp v24, v13 quad_perm:[1,0,3,2] row_mask:0xf bank_mask:0xf bound_ctrl:1
	v_mov_b32_dpp v25, v12 quad_perm:[1,0,3,2] row_mask:0xf bank_mask:0xf bound_ctrl:1
	v_cndmask_b32_e32 v12, v12, v24, vcc
	v_cndmask_b32_e32 v13, v25, v13, vcc
	v_mov_b32_dpp v24, v15 quad_perm:[1,0,3,2] row_mask:0xf bank_mask:0xf bound_ctrl:1
	v_mov_b32_dpp v25, v14 quad_perm:[1,0,3,2] row_mask:0xf bank_mask:0xf bound_ctrl:1
	v_cndmask_b32_e32 v14, v14, v24, vcc
	v_cndmask_b32_e32 v15, v25, v15, vcc
	v_mov_b32_dpp v24, v17 quad_perm:[1,0,3,2] row_mask:0xf bank_mask:0xf bound_ctrl:1
	v_mov_b32_dpp v25, v16 quad_perm:[1,0,3,2] row_mask:0xf bank_mask:0xf bound_ctrl:1
	v_cndmask_b32_e32 v16, v16, v24, vcc
	v_cndmask_b32_e32 v17, v25, v17, vcc
	v_mov_b32_dpp v24, v4 quad_perm:[2,3,0,1] row_mask:0xf bank_mask:0xf bound_ctrl:1
	v_mov_b32_dpp v25, v2 quad_perm:[2,3,0,1] row_mask:0xf bank_mask:0xf bound_ctrl:1
	v_cndmask_b32_e64 v2, v2, v24, s[30:31]
	v_cndmask_b32_e64 v4, v25, v4, s[30:31]
	v_mov_b32_dpp v24, v5 quad_perm:[2,3,0,1] row_mask:0xf bank_mask:0xf bound_ctrl:1
	v_mov_b32_dpp v25, v3 quad_perm:[2,3,0,1] row_mask:0xf bank_mask:0xf bound_ctrl:1
	v_cndmask_b32_e64 v3, v3, v24, s[30:31]
	v_cndmask_b32_e64 v5, v25, v5, s[30:31]
	v_mov_b32_dpp v24, v8 quad_perm:[2,3,0,1] row_mask:0xf bank_mask:0xf bound_ctrl:1
	v_mov_b32_dpp v25, v6 quad_perm:[2,3,0,1] row_mask:0xf bank_mask:0xf bound_ctrl:1
	v_cndmask_b32_e64 v6, v6, v24, s[30:31]
	v_cndmask_b32_e64 v8, v25, v8, s[30:31]
	v_mov_b32_dpp v24, v9 quad_perm:[2,3,0,1] row_mask:0xf bank_mask:0xf bound_ctrl:1
	v_mov_b32_dpp v25, v7 quad_perm:[2,3,0,1] row_mask:0xf bank_mask:0xf bound_ctrl:1
	v_cndmask_b32_e64 v7, v7, v24, s[30:31]
	v_cndmask_b32_e64 v9, v25, v9, s[30:31]
	v_mov_b32_dpp v24, v12 quad_perm:[2,3,0,1] row_mask:0xf bank_mask:0xf bound_ctrl:1
	v_mov_b32_dpp v25, v10 quad_perm:[2,3,0,1] row_mask:0xf bank_mask:0xf bound_ctrl:1
	v_cndmask_b32_e64 v10, v10, v24, s[30:31]
	v_cndmask_b32_e64 v12, v25, v12, s[30:31]
	v_mov_b32_dpp v24, v13 quad_perm:[2,3,0,1] row_mask:0xf bank_mask:0xf bound_ctrl:1
	v_mov_b32_dpp v25, v11 quad_perm:[2,3,0,1] row_mask:0xf bank_mask:0xf bound_ctrl:1
	v_cndmask_b32_e64 v11, v11, v24, s[30:31]
	v_cndmask_b32_e64 v13, v25, v13, s[30:31]
	v_mov_b32_dpp v24, v16 quad_perm:[2,3,0,1] row_mask:0xf bank_mask:0xf bound_ctrl:1
	v_mov_b32_dpp v25, v14 quad_perm:[2,3,0,1] row_mask:0xf bank_mask:0xf bound_ctrl:1
	v_cndmask_b32_e64 v14, v14, v24, s[30:31]
	v_cndmask_b32_e64 v16, v25, v16, s[30:31]
	v_mov_b32_dpp v24, v17 quad_perm:[2,3,0,1] row_mask:0xf bank_mask:0xf bound_ctrl:1
	v_mov_b32_dpp v25, v15 quad_perm:[2,3,0,1] row_mask:0xf bank_mask:0xf bound_ctrl:1
	v_cndmask_b32_e64 v15, v15, v24, s[30:31]
	v_cndmask_b32_e64 v17, v25, v17, s[30:31]
	global_store_dwordx4 v[22:23], v[2:5], off
	global_store_dwordx4 v[22:23], v[6:9], off offset:1024
	global_store_dwordx4 v[22:23], v[10:13], off offset:2048
	global_store_dwordx4 v[22:23], v[14:17], off offset:3072
